# baseline (speedup 1.0000x reference)
.LBB3_2:
	s_load_dword s0, s[0:1], 0x20
	s_and_b32 s14, s2, 7
	v_cvt_f32_ubyte0_e32 v3, s14
	v_lshlrev_b32_e32 v100, 4, v0
	s_mov_b64 s[18:19], 0x20080
	s_waitcnt lgkmcnt(0)
	s_ashr_i32 s1, s0, 31
	s_lshr_b32 s1, s1, 22
	s_add_i32 s1, s0, s1
	s_ashr_i32 s3, s1, 10
	v_cvt_f32_i32_e32 v1, s3
	s_ashr_i32 s1, s1, 31
	s_or_b32 s1, s1, 1
	s_movk_i32 s17, 0x70
	v_rcp_iflag_f32_e32 v2, v1
	s_nop 0
	v_mul_f32_e32 v2, v3, v2
	v_trunc_f32_e32 v2, v2
	v_fma_f32 v3, -v2, v1, v3
	v_cvt_i32_f32_e32 v2, v2
	v_cmp_ge_f32_e64 s[12:13], |v3|, |v1|
	s_and_b64 s[12:13], s[12:13], exec
	s_cselect_b32 s1, s1, 0
	v_readfirstlane_b32 s13, v2
	s_add_i32 s1, s13, s1
	s_lshl_b32 s12, s2, 4
	s_bfe_i32 s13, s1, 0x160000
	s_mul_i32 s1, s1, s3
	s_and_b32 s12, s12, 0x180
	s_sub_i32 s3, s14, s1
	s_lshl_b32 s1, s13, 9
	s_or_b32 s1, s1, s12
	s_lshl_b32 s2, s2, 2
	v_lshrrev_b32_e32 v1, 3, v0
	v_lshrrev_b32_e32 v2, 4, v0
	s_lshl_b32 s3, s3, 10
	s_and_b32 s2, s2, 0xffffff80
	v_xor_b32_e32 v10, v2, v0
	v_or_b32_e32 v2, s1, v1
	s_add_i32 s2, s3, s2
	v_ashrrev_i32_e32 v3, 31, v2
	v_lshlrev_b64 v[4:5], 11, v[2:3]
	v_or_b32_e32 v2, s2, v1
	v_mov_b32_e32 v3, 0
	v_lshlrev_b32_e32 v1, 4, v10
	v_lshlrev_b64 v[6:7], 11, v[2:3]
	v_and_b32_e32 v2, 0x70, v1
	v_add_u32_e32 v1, 0, v100
	v_lshl_add_u64 v[8:9], s[6:7], 0, v[6:7]
	v_lshl_add_u64 v[4:5], s[4:5], 0, v[4:5]
	v_readfirstlane_b32 s6, v1
	v_add_u32_e32 v10, 0x2000, v1
	v_lshl_add_u64 v[6:7], v[4:5], 0, v[2:3]
	v_lshl_add_u64 v[4:5], v[8:9], 0, v[2:3]
	v_add_u32_e32 v2, 0x4000, v1
	s_mov_b32 m0, s6
	s_mov_b64 s[12:13], 0x20000
	v_readfirstlane_b32 s3, v10
	global_load_lds_dwordx4 v[6:7], off
	v_lshl_add_u64 v[8:9], v[6:7], 0, s[12:13]
	s_mov_b32 m0, s3
	v_readfirstlane_b32 s4, v2
	v_add_u32_e32 v2, 0x6000, v1
	global_load_lds_dwordx4 v[8:9], off
	s_mov_b32 m0, s4
	v_readfirstlane_b32 s5, v2
	v_add_u32_e32 v12, 0x8000, v1
	global_load_lds_dwordx4 v[4:5], off
	v_lshl_add_u64 v[8:9], v[4:5], 0, s[12:13]
	s_mov_b32 m0, s5
	s_mov_b64 s[12:13], 0x80
	v_readfirstlane_b32 s16, v12
	v_add_u32_e32 v12, 0xa000, v1
	global_load_lds_dwordx4 v[8:9], off
	v_lshl_add_u64 v[8:9], v[4:5], 0, s[12:13]
	v_add_u32_e32 v2, 0xc000, v1
	v_lshl_add_u64 v[10:11], v[6:7], 0, s[12:13]
	s_mov_b32 m0, s16
	v_readfirstlane_b32 s13, v12
	global_load_lds_dwordx4 v[10:11], off
	v_lshl_add_u64 v[10:11], v[6:7], 0, s[18:19]
	s_mov_b32 m0, s13
	v_readfirstlane_b32 s14, v2
	v_add_u32_e32 v2, 0xe000, v1
	global_load_lds_dwordx4 v[10:11], off
	s_mov_b32 m0, s14
	v_readfirstlane_b32 s15, v2
	s_add_i32 s7, 0, 0x14000
	v_add_u32_e32 v12, 0x10000, v1
	global_load_lds_dwordx4 v[8:9], off
	v_lshl_add_u64 v[8:9], v[4:5], 0, s[18:19]
	s_mov_b32 m0, s15
	s_mov_b64 s[18:19], 0x100
	v_add_u32_e32 v2, s7, v100
	v_readfirstlane_b32 s7, v12
	v_add_u32_e32 v1, 0x12000, v1
	global_load_lds_dwordx4 v[8:9], off
	v_lshl_add_u64 v[8:9], v[4:5], 0, s[18:19]
	v_lshl_add_u64 v[10:11], v[6:7], 0, s[18:19]
	s_mov_b32 m0, s7
	s_mov_b64 s[18:19], 0x20100
	v_readfirstlane_b32 s7, v1
	global_load_lds_dwordx4 v[10:11], off
	v_lshl_add_u64 v[10:11], v[6:7], 0, s[18:19]
	s_mov_b32 m0, s7
	v_readfirstlane_b32 s7, v2
	v_add_u32_e32 v1, 0x2000, v2
	global_load_lds_dwordx4 v[10:11], off
	s_mov_b32 m0, s7
	v_readfirstlane_b32 s12, v1
	global_load_lds_dwordx4 v[8:9], off
	v_lshl_add_u64 v[8:9], v[4:5], 0, s[18:19]
	s_mov_b32 m0, s12
	v_lshrrev_b32_e32 v1, 2, v0
	global_load_lds_dwordx4 v[8:9], off
	v_and_b32_e32 v8, 15, v0
	v_and_b32_e32 v1, 0x60, v1
	v_or_b32_e32 v10, v1, v8
	v_lshlrev_b32_e32 v101, 7, v10
	v_lshlrev_b32_e32 v10, 7, v0
	v_and_b32_e32 v2, 63, v0
	v_lshlrev_b32_e32 v9, 3, v0
	v_and_b32_e32 v102, 0x2780, v10
	v_bitop3_b32 v10, v2, s17, v9 bitop3:0x48
	v_add_u32_e32 v56, 0, v102
	v_add_u32_e32 v48, 0, v101
	s_waitcnt vmcnt(8) lgkmcnt(0)
	s_barrier
	v_add_u32_e32 v2, v56, v10
	v_add_u32_e32 v11, v48, v10
	v_bitop3_b32 v9, v0, v9, 63 bitop3:0x6c
	v_mov_b32_e32 v10, 0x70
	ds_read_b128 v[12:15], v2 offset:16384
	ds_read_b128 v[16:19], v2 offset:18432
	ds_read_b128 v[20:23], v11
	ds_read_b128 v[24:27], v11 offset:2048
	ds_read_b128 v[32:35], v2 offset:20480
	ds_read_b128 v[40:43], v2 offset:22528
	v_bitop3_b32 v103, v9, 64, v10 bitop3:0x6c
	v_add_u32_e32 v10, v48, v103
	v_add_u32_e32 v9, v56, v103
	ds_read_b128 v[48:51], v10
	ds_read_b128 v[52:55], v10 offset:2048
	ds_read_b128 v[56:59], v9 offset:16384
	ds_read_b128 v[60:63], v9 offset:18432
	ds_read_b128 v[64:67], v9 offset:20480
	ds_read_b128 v[68:71], v9 offset:22528
	s_waitcnt lgkmcnt(6)
	v_mfma_f32_16x16x32_f16 v[28:31], v[12:15], v[20:23], 0
	v_mfma_f32_16x16x32_f16 v[36:39], v[16:19], v[20:23], 0
	v_mfma_f32_16x16x32_f16 v[44:47], v[32:35], v[20:23], 0
	v_mfma_f32_16x16x32_f16 v[20:23], v[40:43], v[20:23], 0
	v_mfma_f32_16x16x32_f16 v[12:15], v[12:15], v[24:27], 0
	v_mfma_f32_16x16x32_f16 v[16:19], v[16:19], v[24:27], 0
	v_mfma_f32_16x16x32_f16 v[32:35], v[32:35], v[24:27], 0
	v_mfma_f32_16x16x32_f16 v[24:27], v[40:43], v[24:27], 0
	s_mov_b64 s[18:19], 0x180
	s_mov_b32 m0, s6
	s_waitcnt vmcnt(4) lgkmcnt(0)
	s_barrier
	v_lshl_add_u64 v[40:41], v[4:5], 0, s[18:19]
	v_lshl_add_u64 v[42:43], v[6:7], 0, s[18:19]
	s_mov_b64 s[18:19], 0x20180
	global_load_lds_dwordx4 v[42:43], off
	v_lshl_add_u64 v[42:43], v[6:7], 0, s[18:19]
	s_mov_b32 m0, s3
	s_nop 0
	global_load_lds_dwordx4 v[42:43], off
	s_mov_b32 m0, s4
	s_nop 0
	global_load_lds_dwordx4 v[40:41], off
	v_lshl_add_u64 v[40:41], v[4:5], 0, s[18:19]
	s_mov_b32 m0, s5
	s_nop 0
	global_load_lds_dwordx4 v[40:41], off
	ds_read_b128 v[40:43], v11 offset:32768
	ds_read_b128 v[72:75], v11 offset:34816
	ds_read_b128 v[76:79], v2 offset:49152
	ds_read_b128 v[80:83], v2 offset:51200
	ds_read_b128 v[84:87], v2 offset:53248
	ds_read_b128 v[88:91], v2 offset:55296
	v_mfma_f32_16x16x32_f16 v[28:31], v[56:59], v[48:51], v[28:31]
	v_mfma_f32_16x16x32_f16 v[36:39], v[60:63], v[48:51], v[36:39]
	v_mfma_f32_16x16x32_f16 v[44:47], v[64:67], v[48:51], v[44:47]
	v_mfma_f32_16x16x32_f16 v[20:23], v[68:71], v[48:51], v[20:23]
	v_mfma_f32_16x16x32_f16 v[12:15], v[56:59], v[52:55], v[12:15]
	v_mfma_f32_16x16x32_f16 v[16:19], v[60:63], v[52:55], v[16:19]
	v_mfma_f32_16x16x32_f16 v[32:35], v[64:67], v[52:55], v[32:35]
	v_mfma_f32_16x16x32_f16 v[24:27], v[68:71], v[52:55], v[24:27]
	s_waitcnt lgkmcnt(0)
	v_mfma_f32_16x16x32_f16 v[28:31], v[76:79], v[40:43], v[28:31]
	ds_read_b128 v[52:55], v10 offset:32768
	ds_read_b128 v[56:59], v10 offset:34816
	v_mfma_f32_16x16x32_f16 v[36:39], v[80:83], v[40:43], v[36:39]
	v_mfma_f32_16x16x32_f16 v[44:47], v[84:87], v[40:43], v[44:47]
	v_mfma_f32_16x16x32_f16 v[20:23], v[88:91], v[40:43], v[20:23]
	v_mfma_f32_16x16x32_f16 v[40:43], v[76:79], v[72:75], v[12:15]
	ds_read_b128 v[60:63], v9 offset:49152
	ds_read_b128 v[64:67], v9 offset:51200
	ds_read_b128 v[68:71], v9 offset:53248
	ds_read_b128 v[76:79], v9 offset:55296
	v_mfma_f32_16x16x32_f16 v[48:51], v[80:83], v[72:75], v[16:19]
	v_mfma_f32_16x16x32_f16 v[32:35], v[84:87], v[72:75], v[32:35]
	v_mfma_f32_16x16x32_f16 v[24:27], v[88:91], v[72:75], v[24:27]
	s_mov_b64 s[18:19], 0x200
	s_mov_b32 m0, s16
	s_waitcnt vmcnt(4) lgkmcnt(0)
	s_barrier
	v_lshl_add_u64 v[12:13], v[4:5], 0, s[18:19]
	v_lshl_add_u64 v[14:15], v[6:7], 0, s[18:19]
	s_mov_b64 s[18:19], 0x20200
	global_load_lds_dwordx4 v[14:15], off
	v_lshl_add_u64 v[14:15], v[6:7], 0, s[18:19]
	s_mov_b32 m0, s13
	v_add_u32_e32 v16, 0x15000, v2
	global_load_lds_dwordx4 v[14:15], off
	s_mov_b32 m0, s14
	v_add_u32_e32 v14, 0x14000, v2
	global_load_lds_dwordx4 v[12:13], off
	v_lshl_add_u64 v[12:13], v[4:5], 0, s[18:19]
	s_mov_b32 m0, s15
	v_add_u32_e32 v15, 0x14800, v2
	global_load_lds_dwordx4 v[12:13], off
	v_add_u32_e32 v12, 0x10000, v11
	v_add_u32_e32 v13, 0x10800, v11
	ds_read_b128 v[72:75], v12
	ds_read_b128 v[80:83], v13
	ds_read_b128 v[84:87], v14
	ds_read_b128 v[88:91], v15
	v_add_u32_e32 v17, 0x15800, v2
	ds_read_b128 v[92:95], v16
	ds_read_b128 v[96:99], v17
	v_mfma_f32_16x16x32_f16 v[28:31], v[60:63], v[52:55], v[28:31]
	v_mfma_f32_16x16x32_f16 v[36:39], v[64:67], v[52:55], v[36:39]
	v_mfma_f32_16x16x32_f16 v[44:47], v[68:71], v[52:55], v[44:47]
	v_mfma_f32_16x16x32_f16 v[18:21], v[76:79], v[52:55], v[20:23]
	v_mfma_f32_16x16x32_f16 v[40:43], v[60:63], v[56:59], v[40:43]
	v_mfma_f32_16x16x32_f16 v[48:51], v[64:67], v[56:59], v[48:51]
	v_mfma_f32_16x16x32_f16 v[32:35], v[68:71], v[56:59], v[32:35]
	v_mfma_f32_16x16x32_f16 v[22:25], v[76:79], v[56:59], v[24:27]
	s_add_i32 s17, 0, 0x10000
	s_waitcnt lgkmcnt(0)
	v_mfma_f32_16x16x32_f16 v[52:55], v[96:99], v[72:75], v[18:21]
	s_nop 2
	v_add_u32_e32 v18, s17, v103
	v_add_u32_e32 v19, v18, v101
	v_add_u32_e32 v18, v18, v102
	v_mfma_f32_16x16x32_f16 v[26:29], v[84:87], v[72:75], v[28:31]
	ds_read_b128 v[56:59], v19
	ds_read_b128 v[60:63], v19 offset:2048
	v_mfma_f32_16x16x32_f16 v[36:39], v[88:91], v[72:75], v[36:39]
	v_mfma_f32_16x16x32_f16 v[44:47], v[92:95], v[72:75], v[44:47]
	ds_read_b128 v[64:67], v18 offset:16384
	ds_read_b128 v[68:71], v18 offset:18432
	ds_read_b128 v[72:75], v18 offset:20480
	ds_read_b128 v[76:79], v18 offset:22528
	v_mfma_f32_16x16x32_f16 v[40:43], v[84:87], v[80:83], v[40:43]
	v_mfma_f32_16x16x32_f16 v[48:51], v[88:91], v[80:83], v[48:51]
	v_mfma_f32_16x16x32_f16 v[30:33], v[92:95], v[80:83], v[32:35]
	v_mfma_f32_16x16x32_f16 v[20:23], v[96:99], v[80:83], v[22:25]
	s_mov_b64 s[18:19], 0x280
	v_add_u32_e32 v80, s17, v100
	s_nop 0
	v_lshl_add_u64 v[24:25], v[4:5], 0, s[18:19]
	v_lshl_add_u64 v[34:35], v[6:7], 0, s[18:19]
	v_readfirstlane_b32 s18, v80
	v_add_u32_e32 v80, 0x2000, v80
	s_waitcnt vmcnt(4) lgkmcnt(0)
	s_barrier
	s_mov_b32 m0, s18
	s_mov_b64 s[20:21], 0x20280
	v_readfirstlane_b32 s17, v80
	global_load_lds_dwordx4 v[34:35], off
	v_lshl_add_u64 v[34:35], v[6:7], 0, s[20:21]
	s_mov_b32 m0, s17
	s_nop 0
	global_load_lds_dwordx4 v[34:35], off
	s_mov_b32 m0, s7
	s_nop 0
	global_load_lds_dwordx4 v[24:25], off
	v_lshl_add_u64 v[24:25], v[4:5], 0, s[20:21]
	s_mov_b32 m0, s12
	s_nop 0
	global_load_lds_dwordx4 v[24:25], off
	ds_read_b128 v[80:83], v11
	ds_read_b128 v[84:87], v11 offset:2048
	ds_read_b128 v[88:91], v2 offset:16384
	ds_read_b128 v[92:95], v2 offset:18432
	ds_read_b128 v[96:99], v2 offset:20480
	ds_read_b128 v[100:103], v2 offset:22528
	v_mfma_f32_16x16x32_f16 v[24:27], v[64:67], v[56:59], v[26:29]
	v_mfma_f32_16x16x32_f16 v[34:37], v[68:71], v[56:59], v[36:39]
	v_mfma_f32_16x16x32_f16 v[44:47], v[72:75], v[56:59], v[44:47]
	v_mfma_f32_16x16x32_f16 v[52:55], v[76:79], v[56:59], v[52:55]
	v_mfma_f32_16x16x32_f16 v[38:41], v[64:67], v[60:63], v[40:43]
	v_mfma_f32_16x16x32_f16 v[48:51], v[68:71], v[60:63], v[48:51]
	v_mfma_f32_16x16x32_f16 v[28:31], v[72:75], v[60:63], v[30:33]
	v_mfma_f32_16x16x32_f16 v[20:23], v[76:79], v[60:63], v[20:23]
	ds_read_b128 v[56:59], v10
	ds_read_b128 v[60:63], v10 offset:2048
	ds_read_b128 v[64:67], v9 offset:16384
	ds_read_b128 v[68:71], v9 offset:18432
	ds_read_b128 v[72:75], v9 offset:20480
	ds_read_b128 v[76:79], v9 offset:22528
	s_waitcnt lgkmcnt(6)
	v_mfma_f32_16x16x32_f16 v[24:27], v[88:91], v[80:83], v[24:27]
	v_mfma_f32_16x16x32_f16 v[32:35], v[92:95], v[80:83], v[34:37]
	v_mfma_f32_16x16x32_f16 v[42:45], v[96:99], v[80:83], v[44:47]
	v_mfma_f32_16x16x32_f16 v[52:55], v[100:103], v[80:83], v[52:55]
	v_mfma_f32_16x16x32_f16 v[36:39], v[88:91], v[84:87], v[38:41]
	v_mfma_f32_16x16x32_f16 v[46:49], v[92:95], v[84:87], v[48:51]
	v_mfma_f32_16x16x32_f16 v[28:31], v[96:99], v[84:87], v[28:31]
	v_mfma_f32_16x16x32_f16 v[20:23], v[100:103], v[84:87], v[20:23]
	s_mov_b64 s[20:21], 0x300
	s_mov_b32 m0, s6
	s_waitcnt vmcnt(4) lgkmcnt(0)
	s_barrier
	v_lshl_add_u64 v[40:41], v[4:5], 0, s[20:21]
	v_lshl_add_u64 v[50:51], v[6:7], 0, s[20:21]
	s_mov_b64 s[20:21], 0x20300
	global_load_lds_dwordx4 v[50:51], off
	v_lshl_add_u64 v[50:51], v[6:7], 0, s[20:21]
	s_mov_b32 m0, s3
	s_nop 0
	global_load_lds_dwordx4 v[50:51], off
	s_mov_b32 m0, s4
	s_nop 0
	global_load_lds_dwordx4 v[40:41], off
	v_lshl_add_u64 v[40:41], v[4:5], 0, s[20:21]
	s_mov_b32 m0, s5
	s_nop 0
	global_load_lds_dwordx4 v[40:41], off
	ds_read_b128 v[80:83], v11 offset:32768
	ds_read_b128 v[84:87], v11 offset:34816
	ds_read_b128 v[88:91], v2 offset:49152
	ds_read_b128 v[92:95], v2 offset:51200
	ds_read_b128 v[96:99], v2 offset:53248
	ds_read_b128 v[100:103], v2 offset:55296
	v_mfma_f32_16x16x32_f16 v[24:27], v[64:67], v[56:59], v[24:27]
	v_mfma_f32_16x16x32_f16 v[32:35], v[68:71], v[56:59], v[32:35]
	v_mfma_f32_16x16x32_f16 v[40:43], v[72:75], v[56:59], v[42:45]
	v_mfma_f32_16x16x32_f16 v[50:53], v[76:79], v[56:59], v[52:55]
	v_mfma_f32_16x16x32_f16 v[36:39], v[64:67], v[60:63], v[36:39]
	v_mfma_f32_16x16x32_f16 v[44:47], v[68:71], v[60:63], v[46:49]
	v_mfma_f32_16x16x32_f16 v[28:31], v[72:75], v[60:63], v[28:31]
	v_mfma_f32_16x16x32_f16 v[20:23], v[76:79], v[60:63], v[20:23]
	s_waitcnt lgkmcnt(0)
	v_mfma_f32_16x16x32_f16 v[48:51], v[100:103], v[80:83], v[50:53]
	s_nop 2
	ds_read_b128 v[52:55], v10 offset:32768
	ds_read_b128 v[56:59], v10 offset:34816
	ds_read_b128 v[60:63], v9 offset:49152
	ds_read_b128 v[64:67], v9 offset:51200
	ds_read_b128 v[68:71], v9 offset:53248
	ds_read_b128 v[72:75], v9 offset:55296
	v_mfma_f32_16x16x32_f16 v[24:27], v[88:91], v[80:83], v[24:27]
	v_mfma_f32_16x16x32_f16 v[32:35], v[92:95], v[80:83], v[32:35]
	v_mfma_f32_16x16x32_f16 v[40:43], v[96:99], v[80:83], v[40:43]
	v_mfma_f32_16x16x32_f16 v[36:39], v[88:91], v[84:87], v[36:39]
	v_mfma_f32_16x16x32_f16 v[44:47], v[92:95], v[84:87], v[44:47]
	v_mfma_f32_16x16x32_f16 v[28:31], v[96:99], v[84:87], v[28:31]
	v_mfma_f32_16x16x32_f16 v[20:23], v[100:103], v[84:87], v[20:23]
	s_mov_b64 s[20:21], 0x380
	s_mov_b32 m0, s16
	s_waitcnt vmcnt(4) lgkmcnt(0)
	s_barrier
	v_lshl_add_u64 v[76:77], v[4:5], 0, s[20:21]
	v_lshl_add_u64 v[78:79], v[6:7], 0, s[20:21]
	s_mov_b64 s[20:21], 0x20380
	global_load_lds_dwordx4 v[78:79], off
	v_lshl_add_u64 v[78:79], v[6:7], 0, s[20:21]
	s_mov_b32 m0, s13
	s_nop 0
	global_load_lds_dwordx4 v[78:79], off
	s_mov_b32 m0, s14
	s_nop 0
	global_load_lds_dwordx4 v[76:77], off
	v_lshl_add_u64 v[76:77], v[4:5], 0, s[20:21]
	s_mov_b32 m0, s15
	s_nop 0
	global_load_lds_dwordx4 v[76:77], off
	ds_read_b128 v[76:79], v12
	ds_read_b128 v[80:83], v13
	ds_read_b128 v[84:87], v14
	ds_read_b128 v[88:91], v15
	ds_read_b128 v[92:95], v16
	ds_read_b128 v[96:99], v17
	v_mfma_f32_16x16x32_f16 v[24:27], v[60:63], v[52:55], v[24:27]
	v_mfma_f32_16x16x32_f16 v[32:35], v[64:67], v[52:55], v[32:35]
	v_mfma_f32_16x16x32_f16 v[40:43], v[68:71], v[52:55], v[40:43]
	v_mfma_f32_16x16x32_f16 v[48:51], v[72:75], v[52:55], v[48:51]
	v_mfma_f32_16x16x32_f16 v[36:39], v[60:63], v[56:59], v[36:39]
	v_mfma_f32_16x16x32_f16 v[44:47], v[64:67], v[56:59], v[44:47]
	v_mfma_f32_16x16x32_f16 v[28:31], v[68:71], v[56:59], v[28:31]
	v_mfma_f32_16x16x32_f16 v[20:23], v[72:75], v[56:59], v[20:23]
	ds_read_b128 v[52:55], v19
	ds_read_b128 v[56:59], v19 offset:2048
	ds_read_b128 v[60:63], v18 offset:16384
	ds_read_b128 v[64:67], v18 offset:18432
	ds_read_b128 v[68:71], v18 offset:20480
	ds_read_b128 v[72:75], v18 offset:22528
	s_waitcnt lgkmcnt(6)
	v_mfma_f32_16x16x32_f16 v[24:27], v[84:87], v[76:79], v[24:27]
	v_mfma_f32_16x16x32_f16 v[32:35], v[88:91], v[76:79], v[32:35]
	v_mfma_f32_16x16x32_f16 v[40:43], v[92:95], v[76:79], v[40:43]
	v_mfma_f32_16x16x32_f16 v[48:51], v[96:99], v[76:79], v[48:51]
	v_mfma_f32_16x16x32_f16 v[36:39], v[84:87], v[80:83], v[36:39]
	v_mfma_f32_16x16x32_f16 v[44:47], v[88:91], v[80:83], v[44:47]
	v_mfma_f32_16x16x32_f16 v[28:31], v[92:95], v[80:83], v[28:31]
	v_mfma_f32_16x16x32_f16 v[20:23], v[96:99], v[80:83], v[20:23]
	s_mov_b64 s[20:21], 0x400
	s_mov_b32 m0, s18
	s_waitcnt vmcnt(4) lgkmcnt(0)
	s_barrier
	v_lshl_add_u64 v[76:77], v[4:5], 0, s[20:21]
	v_lshl_add_u64 v[78:79], v[6:7], 0, s[20:21]
	s_mov_b64 s[20:21], 0x20400
	global_load_lds_dwordx4 v[78:79], off
	v_lshl_add_u64 v[78:79], v[6:7], 0, s[20:21]
	s_mov_b32 m0, s17
	s_nop 0
	global_load_lds_dwordx4 v[78:79], off
	s_mov_b32 m0, s7
	s_nop 0
	global_load_lds_dwordx4 v[76:77], off
	v_lshl_add_u64 v[76:77], v[4:5], 0, s[20:21]
	s_mov_b32 m0, s12
	s_nop 0
	global_load_lds_dwordx4 v[76:77], off
	ds_read_b128 v[76:79], v11
	ds_read_b128 v[80:83], v11 offset:2048
	ds_read_b128 v[84:87], v2 offset:16384
	ds_read_b128 v[88:91], v2 offset:18432
	ds_read_b128 v[92:95], v2 offset:20480
	ds_read_b128 v[96:99], v2 offset:22528
	v_mfma_f32_16x16x32_f16 v[24:27], v[60:63], v[52:55], v[24:27]
	v_mfma_f32_16x16x32_f16 v[32:35], v[64:67], v[52:55], v[32:35]
	v_mfma_f32_16x16x32_f16 v[40:43], v[68:71], v[52:55], v[40:43]
	v_mfma_f32_16x16x32_f16 v[48:51], v[72:75], v[52:55], v[48:51]
	v_mfma_f32_16x16x32_f16 v[36:39], v[60:63], v[56:59], v[36:39]
	v_mfma_f32_16x16x32_f16 v[44:47], v[64:67], v[56:59], v[44:47]
	v_mfma_f32_16x16x32_f16 v[28:31], v[68:71], v[56:59], v[28:31]
	v_mfma_f32_16x16x32_f16 v[20:23], v[72:75], v[56:59], v[20:23]
	ds_read_b128 v[52:55], v10
	ds_read_b128 v[56:59], v10 offset:2048
	ds_read_b128 v[60:63], v9 offset:16384
	ds_read_b128 v[64:67], v9 offset:18432
	ds_read_b128 v[68:71], v9 offset:20480
	ds_read_b128 v[72:75], v9 offset:22528
	s_waitcnt lgkmcnt(6)
	v_mfma_f32_16x16x32_f16 v[24:27], v[84:87], v[76:79], v[24:27]
	v_mfma_f32_16x16x32_f16 v[32:35], v[88:91], v[76:79], v[32:35]
	v_mfma_f32_16x16x32_f16 v[40:43], v[92:95], v[76:79], v[40:43]
	v_mfma_f32_16x16x32_f16 v[48:51], v[96:99], v[76:79], v[48:51]
	v_mfma_f32_16x16x32_f16 v[36:39], v[84:87], v[80:83], v[36:39]
	v_mfma_f32_16x16x32_f16 v[44:47], v[88:91], v[80:83], v[44:47]
	v_mfma_f32_16x16x32_f16 v[28:31], v[92:95], v[80:83], v[28:31]
	v_mfma_f32_16x16x32_f16 v[20:23], v[96:99], v[80:83], v[20:23]
	s_mov_b64 s[20:21], 0x480
	s_mov_b32 m0, s6
	s_waitcnt vmcnt(4) lgkmcnt(0)
	s_barrier
	v_lshl_add_u64 v[76:77], v[4:5], 0, s[20:21]
	v_lshl_add_u64 v[78:79], v[6:7], 0, s[20:21]
	s_mov_b64 s[20:21], 0x20480
	global_load_lds_dwordx4 v[78:79], off
	v_lshl_add_u64 v[78:79], v[6:7], 0, s[20:21]
	s_mov_b32 m0, s3
	s_nop 0
	global_load_lds_dwordx4 v[78:79], off
	s_mov_b32 m0, s4
	s_nop 0
	global_load_lds_dwordx4 v[76:77], off
	v_lshl_add_u64 v[76:77], v[4:5], 0, s[20:21]
	s_mov_b32 m0, s5
	s_nop 0
	global_load_lds_dwordx4 v[76:77], off
	ds_read_b128 v[76:79], v11 offset:32768
	ds_read_b128 v[80:83], v11 offset:34816
	ds_read_b128 v[84:87], v2 offset:49152
	ds_read_b128 v[88:91], v2 offset:51200
	ds_read_b128 v[92:95], v2 offset:53248
	ds_read_b128 v[96:99], v2 offset:55296
	v_mfma_f32_16x16x32_f16 v[24:27], v[60:63], v[52:55], v[24:27]
	v_mfma_f32_16x16x32_f16 v[32:35], v[64:67], v[52:55], v[32:35]
	v_mfma_f32_16x16x32_f16 v[40:43], v[68:71], v[52:55], v[40:43]
	v_mfma_f32_16x16x32_f16 v[48:51], v[72:75], v[52:55], v[48:51]
	v_mfma_f32_16x16x32_f16 v[36:39], v[60:63], v[56:59], v[36:39]
	v_mfma_f32_16x16x32_f16 v[44:47], v[64:67], v[56:59], v[44:47]
	v_mfma_f32_16x16x32_f16 v[28:31], v[68:71], v[56:59], v[28:31]
	v_mfma_f32_16x16x32_f16 v[20:23], v[72:75], v[56:59], v[20:23]
	ds_read_b128 v[52:55], v10 offset:32768
	ds_read_b128 v[56:59], v10 offset:34816
	ds_read_b128 v[60:63], v9 offset:49152
	ds_read_b128 v[64:67], v9 offset:51200
	ds_read_b128 v[68:71], v9 offset:53248
	ds_read_b128 v[72:75], v9 offset:55296
	s_waitcnt lgkmcnt(6)
	v_mfma_f32_16x16x32_f16 v[24:27], v[84:87], v[76:79], v[24:27]
	v_mfma_f32_16x16x32_f16 v[32:35], v[88:91], v[76:79], v[32:35]
	v_mfma_f32_16x16x32_f16 v[40:43], v[92:95], v[76:79], v[40:43]
	v_mfma_f32_16x16x32_f16 v[48:51], v[96:99], v[76:79], v[48:51]
	v_mfma_f32_16x16x32_f16 v[36:39], v[84:87], v[80:83], v[36:39]
	v_mfma_f32_16x16x32_f16 v[44:47], v[88:91], v[80:83], v[44:47]
	v_mfma_f32_16x16x32_f16 v[28:31], v[92:95], v[80:83], v[28:31]
	v_mfma_f32_16x16x32_f16 v[20:23], v[96:99], v[80:83], v[20:23]
	s_mov_b64 s[20:21], 0x500
	s_mov_b32 m0, s16
	s_waitcnt vmcnt(4) lgkmcnt(0)
	s_barrier
	v_lshl_add_u64 v[76:77], v[4:5], 0, s[20:21]
	v_lshl_add_u64 v[78:79], v[6:7], 0, s[20:21]
	s_mov_b64 s[20:21], 0x20500
	global_load_lds_dwordx4 v[78:79], off
	v_lshl_add_u64 v[78:79], v[6:7], 0, s[20:21]
	s_mov_b32 m0, s13
	s_nop 0
	global_load_lds_dwordx4 v[78:79], off
	s_mov_b32 m0, s14
	s_nop 0
	global_load_lds_dwordx4 v[76:77], off
	v_lshl_add_u64 v[76:77], v[4:5], 0, s[20:21]
	s_mov_b32 m0, s15
	s_nop 0
	global_load_lds_dwordx4 v[76:77], off
	ds_read_b128 v[76:79], v12
	ds_read_b128 v[80:83], v13
	ds_read_b128 v[84:87], v14
	ds_read_b128 v[88:91], v15
	ds_read_b128 v[92:95], v16
	ds_read_b128 v[96:99], v17
	v_mfma_f32_16x16x32_f16 v[24:27], v[60:63], v[52:55], v[24:27]
	v_mfma_f32_16x16x32_f16 v[32:35], v[64:67], v[52:55], v[32:35]
	v_mfma_f32_16x16x32_f16 v[40:43], v[68:71], v[52:55], v[40:43]
	v_mfma_f32_16x16x32_f16 v[48:51], v[72:75], v[52:55], v[48:51]
	v_mfma_f32_16x16x32_f16 v[36:39], v[60:63], v[56:59], v[36:39]
	v_mfma_f32_16x16x32_f16 v[44:47], v[64:67], v[56:59], v[44:47]
	v_mfma_f32_16x16x32_f16 v[28:31], v[68:71], v[56:59], v[28:31]
	v_mfma_f32_16x16x32_f16 v[20:23], v[72:75], v[56:59], v[20:23]
	ds_read_b128 v[52:55], v19
	ds_read_b128 v[56:59], v19 offset:2048
	ds_read_b128 v[60:63], v18 offset:16384
	ds_read_b128 v[64:67], v18 offset:18432
	ds_read_b128 v[68:71], v18 offset:20480
	ds_read_b128 v[72:75], v18 offset:22528
	s_waitcnt lgkmcnt(6)
	v_mfma_f32_16x16x32_f16 v[24:27], v[84:87], v[76:79], v[24:27]
	v_mfma_f32_16x16x32_f16 v[32:35], v[88:91], v[76:79], v[32:35]
	v_mfma_f32_16x16x32_f16 v[40:43], v[92:95], v[76:79], v[40:43]
	v_mfma_f32_16x16x32_f16 v[48:51], v[96:99], v[76:79], v[48:51]
	v_mfma_f32_16x16x32_f16 v[36:39], v[84:87], v[80:83], v[36:39]
	v_mfma_f32_16x16x32_f16 v[44:47], v[88:91], v[80:83], v[44:47]
	v_mfma_f32_16x16x32_f16 v[28:31], v[92:95], v[80:83], v[28:31]
	v_mfma_f32_16x16x32_f16 v[20:23], v[96:99], v[80:83], v[20:23]
	s_mov_b64 s[20:21], 0x580
	s_mov_b32 m0, s18
	s_waitcnt vmcnt(4) lgkmcnt(0)
	s_barrier
	v_lshl_add_u64 v[76:77], v[4:5], 0, s[20:21]
	v_lshl_add_u64 v[78:79], v[6:7], 0, s[20:21]
	s_mov_b64 s[20:21], 0x20580
	global_load_lds_dwordx4 v[78:79], off
	v_lshl_add_u64 v[78:79], v[6:7], 0, s[20:21]
	s_mov_b32 m0, s17
	s_nop 0
	global_load_lds_dwordx4 v[78:79], off
	s_mov_b32 m0, s7
	s_nop 0
	global_load_lds_dwordx4 v[76:77], off
	v_lshl_add_u64 v[76:77], v[4:5], 0, s[20:21]
	s_mov_b32 m0, s12
	s_nop 0
	global_load_lds_dwordx4 v[76:77], off
	ds_read_b128 v[76:79], v11
	ds_read_b128 v[80:83], v11 offset:2048
	ds_read_b128 v[84:87], v2 offset:16384
	ds_read_b128 v[88:91], v2 offset:18432
	ds_read_b128 v[92:95], v2 offset:20480
	ds_read_b128 v[96:99], v2 offset:22528
	v_mfma_f32_16x16x32_f16 v[24:27], v[60:63], v[52:55], v[24:27]
	v_mfma_f32_16x16x32_f16 v[32:35], v[64:67], v[52:55], v[32:35]
	v_mfma_f32_16x16x32_f16 v[40:43], v[68:71], v[52:55], v[40:43]
	v_mfma_f32_16x16x32_f16 v[48:51], v[72:75], v[52:55], v[48:51]
	v_mfma_f32_16x16x32_f16 v[36:39], v[60:63], v[56:59], v[36:39]
	v_mfma_f32_16x16x32_f16 v[44:47], v[64:67], v[56:59], v[44:47]
	v_mfma_f32_16x16x32_f16 v[28:31], v[68:71], v[56:59], v[28:31]
	v_mfma_f32_16x16x32_f16 v[20:23], v[72:75], v[56:59], v[20:23]
	ds_read_b128 v[52:55], v10
	ds_read_b128 v[56:59], v10 offset:2048
	ds_read_b128 v[60:63], v9 offset:16384
	ds_read_b128 v[64:67], v9 offset:18432
	ds_read_b128 v[68:71], v9 offset:20480
	ds_read_b128 v[72:75], v9 offset:22528
	s_waitcnt lgkmcnt(6)
	v_mfma_f32_16x16x32_f16 v[24:27], v[84:87], v[76:79], v[24:27]
	v_mfma_f32_16x16x32_f16 v[32:35], v[88:91], v[76:79], v[32:35]
	v_mfma_f32_16x16x32_f16 v[40:43], v[92:95], v[76:79], v[40:43]
	v_mfma_f32_16x16x32_f16 v[48:51], v[96:99], v[76:79], v[48:51]
	v_mfma_f32_16x16x32_f16 v[36:39], v[84:87], v[80:83], v[36:39]
	v_mfma_f32_16x16x32_f16 v[44:47], v[88:91], v[80:83], v[44:47]
	v_mfma_f32_16x16x32_f16 v[28:31], v[92:95], v[80:83], v[28:31]
	v_mfma_f32_16x16x32_f16 v[20:23], v[96:99], v[80:83], v[20:23]
	s_mov_b64 s[20:21], 0x600
	s_mov_b32 m0, s6
	s_waitcnt vmcnt(4) lgkmcnt(0)
	s_barrier
	v_lshl_add_u64 v[76:77], v[4:5], 0, s[20:21]
	v_lshl_add_u64 v[78:79], v[6:7], 0, s[20:21]
	s_mov_b64 s[20:21], 0x20600
	global_load_lds_dwordx4 v[78:79], off
	v_lshl_add_u64 v[78:79], v[6:7], 0, s[20:21]
	s_mov_b32 m0, s3
	s_nop 0
	global_load_lds_dwordx4 v[78:79], off
	s_mov_b32 m0, s4
	s_nop 0
	global_load_lds_dwordx4 v[76:77], off
	v_lshl_add_u64 v[76:77], v[4:5], 0, s[20:21]
	s_mov_b32 m0, s5
	s_nop 0
	global_load_lds_dwordx4 v[76:77], off
	ds_read_b128 v[76:79], v11 offset:32768
	ds_read_b128 v[80:83], v11 offset:34816
	ds_read_b128 v[84:87], v2 offset:49152
	ds_read_b128 v[88:91], v2 offset:51200
	ds_read_b128 v[92:95], v2 offset:53248
	ds_read_b128 v[96:99], v2 offset:55296
	v_mfma_f32_16x16x32_f16 v[24:27], v[60:63], v[52:55], v[24:27]
	v_mfma_f32_16x16x32_f16 v[32:35], v[64:67], v[52:55], v[32:35]
	v_mfma_f32_16x16x32_f16 v[40:43], v[68:71], v[52:55], v[40:43]
	v_mfma_f32_16x16x32_f16 v[48:51], v[72:75], v[52:55], v[48:51]
	v_mfma_f32_16x16x32_f16 v[36:39], v[60:63], v[56:59], v[36:39]
	v_mfma_f32_16x16x32_f16 v[44:47], v[64:67], v[56:59], v[44:47]
	v_mfma_f32_16x16x32_f16 v[28:31], v[68:71], v[56:59], v[28:31]
	v_mfma_f32_16x16x32_f16 v[20:23], v[72:75], v[56:59], v[20:23]
	ds_read_b128 v[52:55], v10 offset:32768
	ds_read_b128 v[56:59], v10 offset:34816
	ds_read_b128 v[60:63], v9 offset:49152
	ds_read_b128 v[64:67], v9 offset:51200
	ds_read_b128 v[68:71], v9 offset:53248
	ds_read_b128 v[72:75], v9 offset:55296
	s_waitcnt lgkmcnt(6)
	v_mfma_f32_16x16x32_f16 v[24:27], v[84:87], v[76:79], v[24:27]
	v_mfma_f32_16x16x32_f16 v[32:35], v[88:91], v[76:79], v[32:35]
	v_mfma_f32_16x16x32_f16 v[40:43], v[92:95], v[76:79], v[40:43]
	v_mfma_f32_16x16x32_f16 v[48:51], v[96:99], v[76:79], v[48:51]
	v_mfma_f32_16x16x32_f16 v[36:39], v[84:87], v[80:83], v[36:39]
	v_mfma_f32_16x16x32_f16 v[44:47], v[88:91], v[80:83], v[44:47]
	v_mfma_f32_16x16x32_f16 v[28:31], v[92:95], v[80:83], v[28:31]
	v_mfma_f32_16x16x32_f16 v[20:23], v[96:99], v[80:83], v[20:23]
	s_mov_b64 s[20:21], 0x680
	s_mov_b32 m0, s16
	s_waitcnt vmcnt(4) lgkmcnt(0)
	s_barrier
	v_lshl_add_u64 v[76:77], v[4:5], 0, s[20:21]
	v_lshl_add_u64 v[78:79], v[6:7], 0, s[20:21]
	s_mov_b64 s[20:21], 0x20680
	global_load_lds_dwordx4 v[78:79], off
	v_lshl_add_u64 v[78:79], v[6:7], 0, s[20:21]
	s_mov_b32 m0, s13
	s_nop 0
	global_load_lds_dwordx4 v[78:79], off
	s_mov_b32 m0, s14
	s_nop 0
	global_load_lds_dwordx4 v[76:77], off
	v_lshl_add_u64 v[76:77], v[4:5], 0, s[20:21]
	s_mov_b32 m0, s15
	s_nop 0
	global_load_lds_dwordx4 v[76:77], off
	ds_read_b128 v[76:79], v12
	ds_read_b128 v[80:83], v13
	ds_read_b128 v[84:87], v14
	ds_read_b128 v[88:91], v15
	ds_read_b128 v[92:95], v16
	ds_read_b128 v[96:99], v17
	v_mfma_f32_16x16x32_f16 v[24:27], v[60:63], v[52:55], v[24:27]
	v_mfma_f32_16x16x32_f16 v[32:35], v[64:67], v[52:55], v[32:35]
	v_mfma_f32_16x16x32_f16 v[40:43], v[68:71], v[52:55], v[40:43]
	v_mfma_f32_16x16x32_f16 v[48:51], v[72:75], v[52:55], v[48:51]
	v_mfma_f32_16x16x32_f16 v[36:39], v[60:63], v[56:59], v[36:39]
	v_mfma_f32_16x16x32_f16 v[44:47], v[64:67], v[56:59], v[44:47]
	v_mfma_f32_16x16x32_f16 v[28:31], v[68:71], v[56:59], v[28:31]
	v_mfma_f32_16x16x32_f16 v[20:23], v[72:75], v[56:59], v[20:23]
	ds_read_b128 v[52:55], v19
	ds_read_b128 v[56:59], v19 offset:2048
	ds_read_b128 v[60:63], v18 offset:16384
	ds_read_b128 v[64:67], v18 offset:18432
	ds_read_b128 v[68:71], v18 offset:20480
	ds_read_b128 v[72:75], v18 offset:22528
	s_waitcnt lgkmcnt(6)
	v_mfma_f32_16x16x32_f16 v[24:27], v[84:87], v[76:79], v[24:27]
	v_mfma_f32_16x16x32_f16 v[32:35], v[88:91], v[76:79], v[32:35]
	v_mfma_f32_16x16x32_f16 v[40:43], v[92:95], v[76:79], v[40:43]
	v_mfma_f32_16x16x32_f16 v[48:51], v[96:99], v[76:79], v[48:51]
	v_mfma_f32_16x16x32_f16 v[36:39], v[84:87], v[80:83], v[36:39]
	v_mfma_f32_16x16x32_f16 v[44:47], v[88:91], v[80:83], v[44:47]
	v_mfma_f32_16x16x32_f16 v[28:31], v[92:95], v[80:83], v[28:31]
	v_mfma_f32_16x16x32_f16 v[20:23], v[96:99], v[80:83], v[20:23]
	s_mov_b64 s[14:15], 0x700
	s_mov_b32 m0, s18
	s_waitcnt vmcnt(4) lgkmcnt(0)
	s_barrier
	v_lshl_add_u64 v[76:77], v[4:5], 0, s[14:15]
	v_lshl_add_u64 v[78:79], v[6:7], 0, s[14:15]
	s_mov_b64 s[14:15], 0x20700
	global_load_lds_dwordx4 v[78:79], off
	v_lshl_add_u64 v[78:79], v[6:7], 0, s[14:15]
	s_mov_b32 m0, s17
	s_nop 0
	global_load_lds_dwordx4 v[78:79], off
	s_mov_b32 m0, s7
	s_nop 0
	global_load_lds_dwordx4 v[76:77], off
	v_lshl_add_u64 v[76:77], v[4:5], 0, s[14:15]
	s_mov_b32 m0, s12
	s_nop 0
	global_load_lds_dwordx4 v[76:77], off
	ds_read_b128 v[76:79], v11
	ds_read_b128 v[80:83], v11 offset:2048
	ds_read_b128 v[84:87], v2 offset:16384
	ds_read_b128 v[88:91], v2 offset:18432
	ds_read_b128 v[92:95], v2 offset:20480
	ds_read_b128 v[96:99], v2 offset:22528
	v_mfma_f32_16x16x32_f16 v[24:27], v[60:63], v[52:55], v[24:27]
	v_mfma_f32_16x16x32_f16 v[32:35], v[64:67], v[52:55], v[32:35]
	v_mfma_f32_16x16x32_f16 v[40:43], v[68:71], v[52:55], v[40:43]
	v_mfma_f32_16x16x32_f16 v[48:51], v[72:75], v[52:55], v[48:51]
	v_mfma_f32_16x16x32_f16 v[36:39], v[60:63], v[56:59], v[36:39]
	v_mfma_f32_16x16x32_f16 v[44:47], v[64:67], v[56:59], v[44:47]
	v_mfma_f32_16x16x32_f16 v[28:31], v[68:71], v[56:59], v[28:31]
	v_mfma_f32_16x16x32_f16 v[20:23], v[72:75], v[56:59], v[20:23]
	ds_read_b128 v[52:55], v10
	ds_read_b128 v[56:59], v10 offset:2048
	ds_read_b128 v[60:63], v9 offset:16384
	ds_read_b128 v[64:67], v9 offset:18432
	ds_read_b128 v[68:71], v9 offset:20480
	ds_read_b128 v[72:75], v9 offset:22528
	s_waitcnt lgkmcnt(6)
	v_mfma_f32_16x16x32_f16 v[24:27], v[84:87], v[76:79], v[24:27]
	v_mfma_f32_16x16x32_f16 v[32:35], v[88:91], v[76:79], v[32:35]
	v_mfma_f32_16x16x32_f16 v[40:43], v[92:95], v[76:79], v[40:43]
	v_mfma_f32_16x16x32_f16 v[48:51], v[96:99], v[76:79], v[48:51]
	v_mfma_f32_16x16x32_f16 v[36:39], v[84:87], v[80:83], v[36:39]
	v_mfma_f32_16x16x32_f16 v[44:47], v[88:91], v[80:83], v[44:47]
	v_mfma_f32_16x16x32_f16 v[28:31], v[92:95], v[80:83], v[28:31]
	v_mfma_f32_16x16x32_f16 v[20:23], v[96:99], v[80:83], v[20:23]
	s_mov_b32 m0, s6
	s_mov_b64 s[6:7], 0x780
	s_waitcnt vmcnt(4) lgkmcnt(0)
	s_barrier
	v_lshl_add_u64 v[76:77], v[4:5], 0, s[6:7]
	v_lshl_add_u64 v[78:79], v[6:7], 0, s[6:7]
	s_mov_b64 s[6:7], 0x20780
	global_load_lds_dwordx4 v[78:79], off
	v_lshl_add_u64 v[6:7], v[6:7], 0, s[6:7]
	s_mov_b32 m0, s3
	v_lshl_add_u64 v[4:5], v[4:5], 0, s[6:7]
	global_load_lds_dwordx4 v[6:7], off
	s_mov_b32 m0, s4
	s_nop 0
	global_load_lds_dwordx4 v[76:77], off
	s_mov_b32 m0, s5
	s_nop 0
	global_load_lds_dwordx4 v[4:5], off
	ds_read_b128 v[4:7], v11 offset:32768
	ds_read_b128 v[76:79], v11 offset:34816
	ds_read_b128 v[80:83], v2 offset:49152
	ds_read_b128 v[84:87], v2 offset:51200
	ds_read_b128 v[88:91], v2 offset:53248
	ds_read_b128 v[92:95], v2 offset:55296
	v_mfma_f32_16x16x32_f16 v[24:27], v[60:63], v[52:55], v[24:27]
	v_mfma_f32_16x16x32_f16 v[32:35], v[64:67], v[52:55], v[32:35]
	v_mfma_f32_16x16x32_f16 v[40:43], v[68:71], v[52:55], v[40:43]
	v_mfma_f32_16x16x32_f16 v[48:51], v[72:75], v[52:55], v[48:51]
	v_mfma_f32_16x16x32_f16 v[36:39], v[60:63], v[56:59], v[36:39]
	v_mfma_f32_16x16x32_f16 v[44:47], v[64:67], v[56:59], v[44:47]
	v_mfma_f32_16x16x32_f16 v[28:31], v[68:71], v[56:59], v[28:31]
	v_mfma_f32_16x16x32_f16 v[20:23], v[72:75], v[56:59], v[20:23]
	s_waitcnt lgkmcnt(0)
	v_mfma_f32_16x16x32_f16 v[24:27], v[80:83], v[4:7], v[24:27]
	v_mfma_f32_16x16x32_f16 v[32:35], v[84:87], v[4:7], v[32:35]
	v_mfma_f32_16x16x32_f16 v[40:43], v[88:91], v[4:7], v[40:43]
	v_mfma_f32_16x16x32_f16 v[4:7], v[92:95], v[4:7], v[48:51]
	s_nop 2
	ds_read_b128 v[48:51], v10 offset:32768
	ds_read_b128 v[52:55], v10 offset:34816
	ds_read_b128 v[56:59], v9 offset:49152
	ds_read_b128 v[60:63], v9 offset:51200
	ds_read_b128 v[64:67], v9 offset:53248
	ds_read_b128 v[68:71], v9 offset:55296
	v_mfma_f32_16x16x32_f16 v[36:39], v[80:83], v[76:79], v[36:39]
	v_mfma_f32_16x16x32_f16 v[44:47], v[84:87], v[76:79], v[44:47]
	v_mfma_f32_16x16x32_f16 v[28:31], v[88:91], v[76:79], v[28:31]
	v_mfma_f32_16x16x32_f16 v[20:23], v[92:95], v[76:79], v[20:23]
	s_waitcnt vmcnt(4) lgkmcnt(0)
	s_barrier
	ds_read_b128 v[72:75], v12
	ds_read_b128 v[76:79], v13
	ds_read_b128 v[80:83], v14
	ds_read_b128 v[12:15], v15
	ds_read_b128 v[84:87], v16
	ds_read_b128 v[88:91], v17
	v_mfma_f32_16x16x32_f16 v[24:27], v[56:59], v[48:51], v[24:27]
	v_mfma_f32_16x16x32_f16 v[32:35], v[60:63], v[48:51], v[32:35]
	v_mfma_f32_16x16x32_f16 v[40:43], v[64:67], v[48:51], v[40:43]
	v_mfma_f32_16x16x32_f16 v[4:7], v[68:71], v[48:51], v[4:7]
	v_mfma_f32_16x16x32_f16 v[36:39], v[56:59], v[52:55], v[36:39]
	v_mfma_f32_16x16x32_f16 v[44:47], v[60:63], v[52:55], v[44:47]
	v_mfma_f32_16x16x32_f16 v[28:31], v[64:67], v[52:55], v[28:31]
	v_mfma_f32_16x16x32_f16 v[20:23], v[68:71], v[52:55], v[20:23]
	s_waitcnt lgkmcnt(0)
	v_mfma_f32_16x16x32_f16 v[32:35], v[12:15], v[72:75], v[32:35]
	v_mfma_f32_16x16x32_f16 v[12:15], v[12:15], v[76:79], v[44:47]
	s_nop 2
	ds_read_b128 v[44:47], v19
	ds_read_b128 v[48:51], v19 offset:2048
	ds_read_b128 v[52:55], v18 offset:16384
	ds_read_b128 v[56:59], v18 offset:18432
	ds_read_b128 v[60:63], v18 offset:20480
	ds_read_b128 v[16:19], v18 offset:22528
	v_mfma_f32_16x16x32_f16 v[24:27], v[80:83], v[72:75], v[24:27]
	v_mfma_f32_16x16x32_f16 v[40:43], v[84:87], v[72:75], v[40:43]
	v_mfma_f32_16x16x32_f16 v[4:7], v[88:91], v[72:75], v[4:7]
	v_mfma_f32_16x16x32_f16 v[36:39], v[80:83], v[76:79], v[36:39]
	v_mfma_f32_16x16x32_f16 v[28:31], v[84:87], v[76:79], v[28:31]
	v_mfma_f32_16x16x32_f16 v[20:23], v[88:91], v[76:79], v[20:23]
	s_waitcnt vmcnt(0) lgkmcnt(0)
	s_barrier
	ds_read_b128 v[64:67], v11
	ds_read_b128 v[68:71], v11 offset:2048
	ds_read_b128 v[72:75], v2 offset:16384
	ds_read_b128 v[76:79], v2 offset:18432
	ds_read_b128 v[80:83], v2 offset:20480
	ds_read_b128 v[84:87], v2 offset:22528
	v_mfma_f32_16x16x32_f16 v[24:27], v[52:55], v[44:47], v[24:27]
	v_mfma_f32_16x16x32_f16 v[32:35], v[56:59], v[44:47], v[32:35]
	v_mfma_f32_16x16x32_f16 v[40:43], v[60:63], v[44:47], v[40:43]
	v_mfma_f32_16x16x32_f16 v[4:7], v[16:19], v[44:47], v[4:7]
	v_mfma_f32_16x16x32_f16 v[36:39], v[52:55], v[48:51], v[36:39]
	v_mfma_f32_16x16x32_f16 v[12:15], v[56:59], v[48:51], v[12:15]
	v_mfma_f32_16x16x32_f16 v[28:31], v[60:63], v[48:51], v[28:31]
	v_mfma_f32_16x16x32_f16 v[16:19], v[16:19], v[48:51], v[20:23]
	s_waitcnt lgkmcnt(3)
	v_mfma_f32_16x16x32_f16 v[20:23], v[72:75], v[64:67], v[24:27]
	s_waitcnt lgkmcnt(2)
	v_mfma_f32_16x16x32_f16 v[24:27], v[76:79], v[64:67], v[32:35]
	s_waitcnt lgkmcnt(1)
	v_mfma_f32_16x16x32_f16 v[32:35], v[80:83], v[64:67], v[40:43]
	s_nop 2
	ds_read_b128 v[40:43], v10
	ds_read_b128 v[44:47], v10 offset:2048
	ds_read_b128 v[48:51], v9 offset:16384
	ds_read_b128 v[52:55], v9 offset:18432
	ds_read_b128 v[56:59], v9 offset:20480
	ds_read_b128 v[60:63], v9 offset:22528
	s_waitcnt lgkmcnt(6)
	v_mfma_f32_16x16x32_f16 v[4:7], v[84:87], v[64:67], v[4:7]
	v_mfma_f32_16x16x32_f16 v[36:39], v[72:75], v[68:71], v[36:39]
	v_mfma_f32_16x16x32_f16 v[12:15], v[76:79], v[68:71], v[12:15]
	v_mfma_f32_16x16x32_f16 v[28:31], v[80:83], v[68:71], v[28:31]
	v_mfma_f32_16x16x32_f16 v[16:19], v[84:87], v[68:71], v[16:19]
	s_waitcnt vmcnt(0) lgkmcnt(0)
	s_barrier
	v_and_b32_e32 v2, 64, v0
	v_lshrrev_b32_e32 v9, 6, v0
	v_mfma_f32_16x16x32_f16 v[20:23], v[48:51], v[40:43], v[20:23]
	v_mfma_f32_16x16x32_f16 v[24:27], v[52:55], v[40:43], v[24:27]
	v_mfma_f32_16x16x32_f16 v[32:35], v[56:59], v[40:43], v[32:35]
	v_mfma_f32_16x16x32_f16 v[4:7], v[60:63], v[40:43], v[4:7]
	v_mfma_f32_16x16x32_f16 v[36:39], v[48:51], v[44:47], v[36:39]
	v_mfma_f32_16x16x32_f16 v[10:13], v[52:55], v[44:47], v[12:15]
	v_mfma_f32_16x16x32_f16 v[28:31], v[56:59], v[44:47], v[28:31]
	v_mfma_f32_16x16x32_f16 v[14:17], v[60:63], v[44:47], v[16:19]
	s_movk_i32 s3, 0x2200
	v_mad_u32_u24 v9, v9, s3, 0
	s_nop 0
	v_and_b32_e32 v18, 48, v0
	v_mul_u32_u24_e32 v19, 0x110, v8
	v_add3_u32 v18, v9, v18, v19
	s_barrier
	ds_write_b128 v18, v[20:23]
	ds_write_b128 v18, v[24:27] offset:64
	ds_write_b128 v18, v[32:35] offset:128
	ds_write_b128 v18, v[4:7] offset:192
	ds_write_b128 v18, v[36:39] offset:4352
	ds_write_b128 v18, v[10:13] offset:4416
	ds_write_b128 v18, v[28:31] offset:4480
	ds_write_b128 v18, v[14:17] offset:4544
	v_lshlrev_b32_e32 v4, 2, v8
	v_or3_b32 v2, v4, v2, s2
	v_lshlrev_b64 v[10:11], 2, v[2:3]
	s_waitcnt lgkmcnt(0)
	v_lshl_add_u64 v[2:3], s[10:11], 0, v[10:11]
	global_load_dwordx4 v[2:5], v[2:3], off
	v_bfe_u32 v0, v0, 4, 2
	v_lshlrev_b32_e32 v6, 4, v8
	v_mul_u32_u24_e32 v7, 0x110, v0
	v_add3_u32 v13, v9, v6, v7
	ds_read_b128 v[6:9], v13
	v_or3_b32 v12, s1, v1, v0
	v_mad_i64_i32 v[0:1], s[2:3], v12, s0, 0
	v_lshl_add_u64 v[0:1], v[0:1], 2, s[8:9]
	v_lshl_add_u64 v[0:1], v[0:1], 0, v[10:11]
	v_or_b32_e32 v14, 4, v12
	v_or_b32_e32 v15, 8, v12
	v_or_b32_e32 v16, 12, v12
	v_or_b32_e32 v17, 16, v12
	v_or_b32_e32 v18, 20, v12
	v_or_b32_e32 v19, 24, v12
	v_or_b32_e32 v12, 28, v12
	s_waitcnt vmcnt(0) lgkmcnt(0)
	v_pk_add_f32 v[8:9], v[4:5], v[8:9]
	v_pk_add_f32 v[6:7], v[2:3], v[6:7]
	s_nop 0
	global_store_dwordx4 v[0:1], v[6:9], off sc1
	s_nop 1
	ds_read_b128 v[6:9], v13 offset:1088
	v_mad_i64_i32 v[0:1], s[2:3], v14, s0, 0
	v_lshl_add_u64 v[0:1], v[0:1], 2, s[8:9]
	v_lshl_add_u64 v[0:1], v[0:1], 0, v[10:11]
	s_waitcnt lgkmcnt(0)
	v_pk_add_f32 v[8:9], v[4:5], v[8:9]
	v_pk_add_f32 v[6:7], v[2:3], v[6:7]
	s_nop 0
	global_store_dwordx4 v[0:1], v[6:9], off sc1
	s_nop 1
	ds_read_b128 v[6:9], v13 offset:2176
	v_mad_i64_i32 v[0:1], s[2:3], v15, s0, 0
	v_lshl_add_u64 v[0:1], v[0:1], 2, s[8:9]
	v_lshl_add_u64 v[0:1], v[0:1], 0, v[10:11]
	s_waitcnt lgkmcnt(0)
	v_pk_add_f32 v[8:9], v[4:5], v[8:9]
	v_pk_add_f32 v[6:7], v[2:3], v[6:7]
	s_nop 0
	global_store_dwordx4 v[0:1], v[6:9], off sc1
	s_nop 1
	ds_read_b128 v[6:9], v13 offset:3264
	v_mad_i64_i32 v[0:1], s[2:3], v16, s0, 0
	v_lshl_add_u64 v[0:1], v[0:1], 2, s[8:9]
	v_lshl_add_u64 v[0:1], v[0:1], 0, v[10:11]
	s_waitcnt lgkmcnt(0)
	v_pk_add_f32 v[8:9], v[4:5], v[8:9]
	v_pk_add_f32 v[6:7], v[2:3], v[6:7]
	s_nop 0
	global_store_dwordx4 v[0:1], v[6:9], off sc1
	s_nop 1
	ds_read_b128 v[6:9], v13 offset:4352
	v_mad_i64_i32 v[0:1], s[2:3], v17, s0, 0
	v_lshl_add_u64 v[0:1], v[0:1], 2, s[8:9]
	v_lshl_add_u64 v[0:1], v[0:1], 0, v[10:11]
	s_waitcnt lgkmcnt(0)
	v_pk_add_f32 v[8:9], v[4:5], v[8:9]
	v_pk_add_f32 v[6:7], v[2:3], v[6:7]
	s_nop 0
	global_store_dwordx4 v[0:1], v[6:9], off sc1
	s_nop 1
	ds_read_b128 v[6:9], v13 offset:5440
	v_mad_i64_i32 v[0:1], s[2:3], v18, s0, 0
	v_lshl_add_u64 v[0:1], v[0:1], 2, s[8:9]
	v_lshl_add_u64 v[0:1], v[0:1], 0, v[10:11]
	s_waitcnt lgkmcnt(0)
	v_pk_add_f32 v[8:9], v[4:5], v[8:9]
	v_pk_add_f32 v[6:7], v[2:3], v[6:7]
	s_nop 0
	global_store_dwordx4 v[0:1], v[6:9], off sc1
	s_nop 1
	ds_read_b128 v[6:9], v13 offset:6528
	v_mad_i64_i32 v[0:1], s[2:3], v19, s0, 0
	v_lshl_add_u64 v[0:1], v[0:1], 2, s[8:9]
	v_lshl_add_u64 v[0:1], v[0:1], 0, v[10:11]
	s_waitcnt lgkmcnt(0)
	v_pk_add_f32 v[8:9], v[4:5], v[8:9]
	v_pk_add_f32 v[6:7], v[2:3], v[6:7]
	s_nop 0
	global_store_dwordx4 v[0:1], v[6:9], off sc1
	s_nop 1
	ds_read_b128 v[6:9], v13 offset:7616
	v_mad_i64_i32 v[0:1], s[0:1], v12, s0, 0
	v_lshl_add_u64 v[0:1], v[0:1], 2, s[8:9]
	v_lshl_add_u64 v[0:1], v[0:1], 0, v[10:11]
	s_waitcnt lgkmcnt(0)
	v_pk_add_f32 v[4:5], v[4:5], v[8:9]
	v_pk_add_f32 v[2:3], v[2:3], v[6:7]
	s_nop 0
	global_store_dwordx4 v[0:1], v[2:5], off sc1
	s_nop 1
	s_endpgm
